# v57 + attention softmax instruction selection: exp2 argument p*C-m as one packed FMA per pair (drops 16 pk_mul + 32 scalar sub per tile in the differential and latent mixers), packed subtract in the d
# baseline (speedup 1.0000x reference)
.LBB6_1219:
	s_nop 8
	s_nop 4
	s_nop 0
	v_max_f32_e32 v205, v91, v75
	v_max_f32_e32 v186, v88, v72
	v_max_f32_e32 v203, v89, v73
	v_max_f32_e32 v204, v90, v74
	v_max3_f32 v205, v87, v71, v205
	v_max3_f32 v186, v84, v68, v186
	v_max3_f32 v203, v85, v69, v203
	v_max3_f32 v204, v86, v70, v204
	v_max3_f32 v205, v95, v79, v205
	v_max3_f32 v186, v92, v76, v186
	v_max3_f32 v203, v93, v77, v203
	v_max3_f32 v204, v94, v78, v204
	v_max_f32_e32 v206, v98, v82
	v_max3_f32 v205, v99, v83, v205
	v_max3_f32 v186, v96, v80, v186
	v_max3_f32 v203, v97, v81, v203
	v_max3_f32 v204, v206, v204, v205
	v_max3_f32 v186, v186, v203, v204
	v_mov_b32_e32 v203, v186
	s_nop 1
	v_permlane32_swap_b32_e32 v186, v203
	v_max_f32_e32 v203, v203, v203
	v_max_f32_e32 v186, v186, v186
	v_max_f32_e32 v186, v186, v203
	v_mul_f32_e32 v186, s40, v186
	v_sub_f32_e32 v203, v186, v188
	v_cmp_ge_f32_e32 vcc, s97, v203
	v_max_f32_e32 v203, v188, v188
	v_max_f32_e32 v203, v203, v186
	v_sub_f32_e32 v186, v188, v203
	v_exp_f32_e32 v186, v186
	s_cmp_eq_u64 vcc, exec
	s_cselect_b64 vcc, -1, 0
	s_cbranch_vccnz .LBB6_1221
	v_pk_mul_f32 v[66:67], v[66:67], v[186:187] op_sel_hi:[1,0]
	v_pk_mul_f32 v[64:65], v[64:65], v[186:187] op_sel_hi:[1,0]
	v_pk_mul_f32 v[62:63], v[62:63], v[186:187] op_sel_hi:[1,0]
	v_pk_mul_f32 v[60:61], v[60:61], v[186:187] op_sel_hi:[1,0]
	v_pk_mul_f32 v[58:59], v[58:59], v[186:187] op_sel_hi:[1,0]
	v_pk_mul_f32 v[56:57], v[56:57], v[186:187] op_sel_hi:[1,0]
	v_pk_mul_f32 v[54:55], v[54:55], v[186:187] op_sel_hi:[1,0]
	v_pk_mul_f32 v[52:53], v[52:53], v[186:187] op_sel_hi:[1,0]
	v_pk_mul_f32 v[50:51], v[50:51], v[186:187] op_sel_hi:[1,0]
	v_pk_mul_f32 v[48:49], v[48:49], v[186:187] op_sel_hi:[1,0]
	v_pk_mul_f32 v[46:47], v[46:47], v[186:187] op_sel_hi:[1,0]
	v_pk_mul_f32 v[44:45], v[44:45], v[186:187] op_sel_hi:[1,0]
	v_pk_mul_f32 v[42:43], v[42:43], v[186:187] op_sel_hi:[1,0]
	v_pk_mul_f32 v[40:41], v[40:41], v[186:187] op_sel_hi:[1,0]
	v_pk_mul_f32 v[38:39], v[38:39], v[186:187] op_sel_hi:[1,0]
	v_pk_mul_f32 v[36:37], v[36:37], v[186:187] op_sel_hi:[1,0]
	v_pk_mul_f32 v[34:35], v[34:35], v[186:187] op_sel_hi:[1,0]
	v_pk_mul_f32 v[32:33], v[32:33], v[186:187] op_sel_hi:[1,0]
	v_pk_mul_f32 v[30:31], v[30:31], v[186:187] op_sel_hi:[1,0]
	v_pk_mul_f32 v[28:29], v[28:29], v[186:187] op_sel_hi:[1,0]
	v_pk_mul_f32 v[26:27], v[26:27], v[186:187] op_sel_hi:[1,0]
	v_pk_mul_f32 v[24:25], v[24:25], v[186:187] op_sel_hi:[1,0]
	v_pk_mul_f32 v[22:23], v[22:23], v[186:187] op_sel_hi:[1,0]
	v_pk_mul_f32 v[20:21], v[20:21], v[186:187] op_sel_hi:[1,0]
	v_pk_mul_f32 v[18:19], v[18:19], v[186:187] op_sel_hi:[1,0]
	v_pk_mul_f32 v[16:17], v[16:17], v[186:187] op_sel_hi:[1,0]
	v_pk_mul_f32 v[14:15], v[14:15], v[186:187] op_sel_hi:[1,0]
	v_pk_mul_f32 v[12:13], v[12:13], v[186:187] op_sel_hi:[1,0]
	v_pk_mul_f32 v[10:11], v[10:11], v[186:187] op_sel_hi:[1,0]
	v_pk_mul_f32 v[8:9], v[8:9], v[186:187] op_sel_hi:[1,0]
	v_pk_mul_f32 v[6:7], v[6:7], v[186:187] op_sel_hi:[1,0]
	v_pk_mul_f32 v[4:5], v[4:5], v[186:187] op_sel_hi:[1,0]
.LBB6_1221:
	v_cndmask_b32_e32 v188, v203, v188, vcc
	v_mov_b32_e32 v210, v188
	v_pk_fma_f32 v[98:99], v[98:99], s[40:41], v[210:211] op_sel_hi:[1,0,0] neg_lo:[0,0,1] neg_hi:[0,0,1]
	v_pk_fma_f32 v[96:97], v[96:97], s[40:41], v[210:211] op_sel_hi:[1,0,0] neg_lo:[0,0,1] neg_hi:[0,0,1]
	v_pk_fma_f32 v[94:95], v[94:95], s[40:41], v[210:211] op_sel_hi:[1,0,0] neg_lo:[0,0,1] neg_hi:[0,0,1]
	v_pk_fma_f32 v[92:93], v[92:93], s[40:41], v[210:211] op_sel_hi:[1,0,0] neg_lo:[0,0,1] neg_hi:[0,0,1]
	v_pk_fma_f32 v[90:91], v[90:91], s[40:41], v[210:211] op_sel_hi:[1,0,0] neg_lo:[0,0,1] neg_hi:[0,0,1]
	v_pk_fma_f32 v[88:89], v[88:89], s[40:41], v[210:211] op_sel_hi:[1,0,0] neg_lo:[0,0,1] neg_hi:[0,0,1]
	v_pk_fma_f32 v[86:87], v[86:87], s[40:41], v[210:211] op_sel_hi:[1,0,0] neg_lo:[0,0,1] neg_hi:[0,0,1]
	v_pk_fma_f32 v[84:85], v[84:85], s[40:41], v[210:211] op_sel_hi:[1,0,0] neg_lo:[0,0,1] neg_hi:[0,0,1]
	v_pk_fma_f32 v[204:205], v[82:83], s[40:41], v[210:211] op_sel_hi:[1,0,0] neg_lo:[0,0,1] neg_hi:[0,0,1]
	v_pk_fma_f32 v[206:207], v[80:81], s[40:41], v[210:211] op_sel_hi:[1,0,0] neg_lo:[0,0,1] neg_hi:[0,0,1]
	v_pk_fma_f32 v[208:209], v[78:79], s[40:41], v[210:211] op_sel_hi:[1,0,0] neg_lo:[0,0,1] neg_hi:[0,0,1]
	v_pk_fma_f32 v[224:225], v[76:77], s[40:41], v[210:211] op_sel_hi:[1,0,0] neg_lo:[0,0,1] neg_hi:[0,0,1]
	v_pk_fma_f32 v[68:69], v[68:69], s[40:41], v[210:211] op_sel_hi:[1,0,0] neg_lo:[0,0,1] neg_hi:[0,0,1]
	v_pk_fma_f32 v[70:71], v[70:71], s[40:41], v[210:211] op_sel_hi:[1,0,0] neg_lo:[0,0,1] neg_hi:[0,0,1]
	v_pk_fma_f32 v[72:73], v[72:73], s[40:41], v[210:211] op_sel_hi:[1,0,0] neg_lo:[0,0,1] neg_hi:[0,0,1]
	v_pk_fma_f32 v[74:75], v[74:75], s[40:41], v[210:211] op_sel_hi:[1,0,0] neg_lo:[0,0,1] neg_hi:[0,0,1]
	v_exp_f32_e32 v76, v68
	v_exp_f32_e32 v68, v84
	v_exp_f32_e32 v77, v69
	v_exp_f32_e32 v69, v85
	v_exp_f32_e32 v78, v70
	v_exp_f32_e32 v70, v86
	v_exp_f32_e32 v79, v71
	v_exp_f32_e32 v71, v87
	v_exp_f32_e32 v80, v72
	v_exp_f32_e32 v72, v88
	v_exp_f32_e32 v81, v73
	v_exp_f32_e32 v73, v89
	v_exp_f32_e32 v82, v74
	v_exp_f32_e32 v74, v90
	v_exp_f32_e32 v83, v75
	v_exp_f32_e32 v75, v91
	v_exp_f32_e32 v84, v92
	v_exp_f32_e32 v86, v224
	v_exp_f32_e32 v85, v93
	v_exp_f32_e32 v87, v225
	v_exp_f32_e32 v88, v94
	v_exp_f32_e32 v90, v208
	v_exp_f32_e32 v89, v95
	v_exp_f32_e32 v91, v209
	v_exp_f32_e32 v92, v96
	v_exp_f32_e32 v94, v206
	v_exp_f32_e32 v93, v97
	v_exp_f32_e32 v95, v207
	v_exp_f32_e32 v96, v98
	v_exp_f32_e32 v98, v204
	v_exp_f32_e32 v97, v99
	v_exp_f32_e32 v99, v205
	v_pk_add_f32 v[204:205], v[90:91], v[88:89]
	v_pk_add_f32 v[206:207], v[78:79], v[70:71]
	v_pk_add_f32 v[210:211], v[82:83], v[74:75]
	v_pk_add_f32 v[208:209], v[98:99], v[96:97]
	v_pk_add_f32 v[216:217], v[86:87], v[84:85]
	v_pk_add_f32 v[218:219], v[76:77], v[68:69]
	v_pk_add_f32 v[220:221], v[94:95], v[92:93]
	v_pk_add_f32 v[222:223], v[80:81], v[72:73]
	v_pk_add_f32 v[216:217], v[218:219], v[216:217]
	v_pk_add_f32 v[220:221], v[222:223], v[220:221]
	v_pk_add_f32 v[208:209], v[210:211], v[208:209]
	v_pk_add_f32 v[204:205], v[206:207], v[204:205]
	v_pk_add_f32 v[206:207], v[216:217], v[220:221]
	v_pk_add_f32 v[204:205], v[204:205], v[208:209]
	v_cndmask_b32_e64 v186, v186, 1.0, vcc
	v_pk_add_f32 v[204:205], v[206:207], v[204:205]
	v_cvt_pk_bf16_f32 v68, v68, v69
	v_add_f32_e32 v203, v204, v205
	v_fmac_f32_e32 v203, v187, v186
	v_cvt_pk_bf16_f32 v69, v70, v71
	v_cvt_pk_bf16_f32 v71, v74, v75
	v_cvt_pk_bf16_f32 v75, v96, v97
	v_add3_u32 v96, s7, v169, v2
	v_add3_u32 v186, s7, v2, v169
	v_cvt_pk_bf16_f32 v70, v72, v73
	v_cvt_pk_bf16_f32 v72, v84, v85
	v_cvt_pk_bf16_f32 v73, v88, v89
	v_cvt_pk_bf16_f32 v74, v92, v93
	v_cvt_pk_bf16_f32 v76, v76, v77
	v_cvt_pk_bf16_f32 v77, v78, v79
	v_cvt_pk_bf16_f32 v78, v80, v81
	v_cvt_pk_bf16_f32 v79, v82, v83
	v_cvt_pk_bf16_f32 v80, v86, v87
	v_cvt_pk_bf16_f32 v81, v90, v91
	v_cvt_pk_bf16_f32 v82, v94, v95
	v_cvt_pk_bf16_f32 v83, v98, v99
	ds_read_b128 v[84:87], v96 offset:25600
	ds_read_b128 v[88:91], v96 offset:25632
	ds_read_b128 v[92:95], v96 offset:25664
	ds_read_b128 v[96:99], v96 offset:25696
	ds_read_b128 v[204:207], v186 offset:30208
	ds_read_b128 v[208:211], v186 offset:30240
	ds_read_b128 v[230:233], v186 offset:30272
	ds_read_b128 v[234:237], v186 offset:30304
	s_waitcnt lgkmcnt(7)
	v_mfma_f32_32x32x16_bf16 v[52:67], v[84:87], v[68:71], v[52:67]
	s_waitcnt lgkmcnt(6)
	v_mfma_f32_32x32x16_bf16 v[52:67], v[88:91], v[72:75], v[52:67]
	s_waitcnt lgkmcnt(5)
	v_mfma_f32_32x32x16_bf16 v[52:67], v[92:95], v[76:79], v[52:67]
	s_waitcnt lgkmcnt(4)
	v_mfma_f32_32x32x16_bf16 v[52:67], v[96:99], v[80:83], v[52:67]
	ds_read_b128 v[84:87], v186 offset:34816
	ds_read_b128 v[88:91], v186 offset:34848
	ds_read_b128 v[92:95], v186 offset:34880
	ds_read_b128 v[96:99], v186 offset:34912
	s_waitcnt lgkmcnt(7)
	v_mfma_f32_32x32x16_bf16 v[36:51], v[204:207], v[68:71], v[36:51]
	s_waitcnt lgkmcnt(6)
	v_mfma_f32_32x32x16_bf16 v[36:51], v[208:211], v[72:75], v[36:51]
	s_waitcnt lgkmcnt(5)
	v_mfma_f32_32x32x16_bf16 v[36:51], v[230:233], v[76:79], v[36:51]
	s_waitcnt lgkmcnt(4)
	v_mfma_f32_32x32x16_bf16 v[36:51], v[234:237], v[80:83], v[36:51]
	ds_read_b128 v[204:207], v186 offset:39424
	ds_read_b128 v[208:211], v186 offset:39456
	ds_read_b128 v[230:233], v186 offset:39488
	ds_read_b128 v[234:237], v186 offset:39520
	s_waitcnt lgkmcnt(7)
	v_mfma_f32_32x32x16_bf16 v[20:35], v[84:87], v[68:71], v[20:35]
	s_waitcnt lgkmcnt(6)
	v_mfma_f32_32x32x16_bf16 v[20:35], v[88:91], v[72:75], v[20:35]
	s_waitcnt lgkmcnt(5)
	v_mfma_f32_32x32x16_bf16 v[20:35], v[92:95], v[76:79], v[20:35]
	s_waitcnt lgkmcnt(4)
	v_mfma_f32_32x32x16_bf16 v[20:35], v[96:99], v[80:83], v[20:35]
	s_waitcnt lgkmcnt(3)
	v_mfma_f32_32x32x16_bf16 v[4:19], v[204:207], v[68:71], v[4:19]
	s_waitcnt lgkmcnt(2)
	v_mfma_f32_32x32x16_bf16 v[4:19], v[208:211], v[72:75], v[4:19]
	s_waitcnt lgkmcnt(1)
	v_mfma_f32_32x32x16_bf16 v[4:19], v[230:233], v[76:79], v[4:19]
	s_waitcnt lgkmcnt(0)
	v_mfma_f32_32x32x16_bf16 v[4:19], v[234:237], v[80:83], v[4:19]
	v_mov_b32_e32 v187, v203

.LBB6_1241:
	v_cndmask_b32_e32 v229, v85, v229, vcc
	v_cndmask_b32_e64 v216, v84, 1.0, vcc
	v_mov_b32_e32 v240, v229
	v_pk_add_f32 v[96:97], v[82:83], v[240:241] op_sel_hi:[1,0] neg_lo:[0,1] neg_hi:[0,1]
	v_pk_add_f32 v[92:93], v[80:81], v[240:241] op_sel_hi:[1,0] neg_lo:[0,1] neg_hi:[0,1]
	v_pk_add_f32 v[88:89], v[78:79], v[240:241] op_sel_hi:[1,0] neg_lo:[0,1] neg_hi:[0,1]
	v_pk_add_f32 v[84:85], v[76:77], v[240:241] op_sel_hi:[1,0] neg_lo:[0,1] neg_hi:[0,1]
	v_pk_add_f32 v[74:75], v[74:75], v[240:241] op_sel_hi:[1,0] neg_lo:[0,1] neg_hi:[0,1]
	v_pk_add_f32 v[72:73], v[72:73], v[240:241] op_sel_hi:[1,0] neg_lo:[0,1] neg_hi:[0,1]
	v_pk_add_f32 v[70:71], v[70:71], v[240:241] op_sel_hi:[1,0] neg_lo:[0,1] neg_hi:[0,1]
	v_pk_add_f32 v[68:69], v[68:69], v[240:241] op_sel_hi:[1,0] neg_lo:[0,1] neg_hi:[0,1]
	v_pk_add_f32 v[98:99], v[130:131], v[240:241] op_sel_hi:[1,0] neg_lo:[0,1] neg_hi:[0,1]
	v_pk_add_f32 v[94:95], v[128:129], v[240:241] op_sel_hi:[1,0] neg_lo:[0,1] neg_hi:[0,1]
	v_pk_add_f32 v[90:91], v[126:127], v[240:241] op_sel_hi:[1,0] neg_lo:[0,1] neg_hi:[0,1]
	v_pk_add_f32 v[86:87], v[124:125], v[240:241] op_sel_hi:[1,0] neg_lo:[0,1] neg_hi:[0,1]
	v_pk_add_f32 v[82:83], v[122:123], v[240:241] op_sel_hi:[1,0] neg_lo:[0,1] neg_hi:[0,1]
	v_pk_add_f32 v[80:81], v[120:121], v[240:241] op_sel_hi:[1,0] neg_lo:[0,1] neg_hi:[0,1]
	v_pk_add_f32 v[78:79], v[118:119], v[240:241] op_sel_hi:[1,0] neg_lo:[0,1] neg_hi:[0,1]
	v_pk_add_f32 v[76:77], v[116:117], v[240:241] op_sel_hi:[1,0] neg_lo:[0,1] neg_hi:[0,1]
	v_exp_f32_e32 v68, v68
	v_exp_f32_e32 v76, v76
	v_exp_f32_e32 v69, v69
	v_exp_f32_e32 v77, v77
	v_exp_f32_e32 v70, v70
	v_exp_f32_e32 v78, v78
	v_exp_f32_e32 v71, v71
	v_exp_f32_e32 v79, v79
	v_exp_f32_e32 v72, v72
	v_exp_f32_e32 v80, v80
	v_exp_f32_e32 v73, v73
	v_exp_f32_e32 v81, v81
	v_exp_f32_e32 v74, v74
	v_exp_f32_e32 v82, v82
	v_exp_f32_e32 v75, v75
	v_exp_f32_e32 v83, v83
	v_exp_f32_e32 v84, v84
	v_exp_f32_e32 v86, v86
	v_exp_f32_e32 v85, v85
	v_exp_f32_e32 v87, v87
	v_exp_f32_e32 v88, v88
	v_exp_f32_e32 v90, v90
	v_exp_f32_e32 v89, v89
	v_exp_f32_e32 v91, v91
	v_exp_f32_e32 v92, v92
	v_exp_f32_e32 v94, v94
	v_exp_f32_e32 v93, v93
	v_exp_f32_e32 v95, v95
	v_exp_f32_e32 v96, v96
	v_exp_f32_e32 v98, v98
	v_exp_f32_e32 v97, v97
	v_exp_f32_e32 v99, v99
	v_pk_add_f32 v[100:101], v[90:91], v[88:89]
	v_pk_add_f32 v[102:103], v[78:79], v[70:71]
	v_pk_add_f32 v[106:107], v[82:83], v[74:75]
	v_pk_add_f32 v[104:105], v[98:99], v[96:97]
	v_pk_add_f32 v[108:109], v[86:87], v[84:85]
	v_pk_add_f32 v[110:111], v[76:77], v[68:69]
	v_pk_add_f32 v[112:113], v[94:95], v[92:93]
	v_pk_add_f32 v[114:115], v[80:81], v[72:73]
	v_pk_add_f32 v[108:109], v[110:111], v[108:109]
	v_pk_add_f32 v[112:113], v[114:115], v[112:113]
	v_pk_add_f32 v[104:105], v[106:107], v[104:105]
	v_pk_add_f32 v[100:101], v[102:103], v[100:101]
	v_pk_add_f32 v[102:103], v[108:109], v[112:113]
	v_pk_add_f32 v[100:101], v[100:101], v[104:105]
	v_cvt_pk_bf16_f32 v68, v68, v69
	v_pk_add_f32 v[100:101], v[102:103], v[100:101]
	v_cvt_pk_bf16_f32 v69, v70, v71
	v_cvt_pk_bf16_f32 v71, v74, v75
	v_cvt_pk_bf16_f32 v75, v96, v97
	v_add3_u32 v96, s48, v238, v2
	v_add3_u32 v117, s48, v2, v238
	v_add_f32_e32 v116, v100, v101
	v_cvt_pk_bf16_f32 v70, v72, v73
	v_cvt_pk_bf16_f32 v72, v84, v85
	v_cvt_pk_bf16_f32 v73, v88, v89
	v_cvt_pk_bf16_f32 v74, v92, v93
	v_cvt_pk_bf16_f32 v76, v76, v77
	v_cvt_pk_bf16_f32 v77, v78, v79
	v_cvt_pk_bf16_f32 v78, v80, v81
	v_cvt_pk_bf16_f32 v79, v82, v83
	v_cvt_pk_bf16_f32 v80, v86, v87
	v_cvt_pk_bf16_f32 v81, v90, v91
	v_cvt_pk_bf16_f32 v82, v94, v95
	v_cvt_pk_bf16_f32 v83, v98, v99
	ds_read_b128 v[84:87], v96 offset:17408
	ds_read_b128 v[88:91], v96 offset:17440
	ds_read_b128 v[92:95], v96 offset:17472
	ds_read_b128 v[96:99], v96 offset:17504
	ds_read_b128 v[100:103], v117 offset:22016
	ds_read_b128 v[104:107], v117 offset:22048
	ds_read_b128 v[108:111], v117 offset:22080
	ds_read_b128 v[112:115], v117 offset:22112
	v_fmac_f32_e32 v116, v230, v216
	s_waitcnt lgkmcnt(7)
	v_mfma_f32_32x32x16_bf16 v[52:67], v[84:87], v[68:71], v[52:67]
	s_waitcnt lgkmcnt(6)
	v_mfma_f32_32x32x16_bf16 v[52:67], v[88:91], v[72:75], v[52:67]
	s_waitcnt lgkmcnt(5)
	v_mfma_f32_32x32x16_bf16 v[52:67], v[92:95], v[76:79], v[52:67]
	s_waitcnt lgkmcnt(4)
	v_mfma_f32_32x32x16_bf16 v[52:67], v[96:99], v[80:83], v[52:67]
	ds_read_b128 v[84:87], v117 offset:26624
	ds_read_b128 v[88:91], v117 offset:26656
	ds_read_b128 v[92:95], v117 offset:26688
	ds_read_b128 v[96:99], v117 offset:26720
	s_waitcnt lgkmcnt(7)
	v_mfma_f32_32x32x16_bf16 v[36:51], v[100:103], v[68:71], v[36:51]
	s_waitcnt lgkmcnt(6)
	v_mfma_f32_32x32x16_bf16 v[36:51], v[104:107], v[72:75], v[36:51]
	s_waitcnt lgkmcnt(5)
	v_mfma_f32_32x32x16_bf16 v[36:51], v[108:111], v[76:79], v[36:51]
	s_waitcnt lgkmcnt(4)
	v_mfma_f32_32x32x16_bf16 v[36:51], v[112:115], v[80:83], v[36:51]
	ds_read_b128 v[100:103], v117 offset:31232
	ds_read_b128 v[104:107], v117 offset:31264
	ds_read_b128 v[108:111], v117 offset:31296
	ds_read_b128 v[112:115], v117 offset:31328
	s_waitcnt lgkmcnt(7)
	v_mfma_f32_32x32x16_bf16 v[20:35], v[84:87], v[68:71], v[20:35]
	s_waitcnt lgkmcnt(6)
	v_mfma_f32_32x32x16_bf16 v[20:35], v[88:91], v[72:75], v[20:35]
	s_waitcnt lgkmcnt(5)
	v_mfma_f32_32x32x16_bf16 v[20:35], v[92:95], v[76:79], v[20:35]
	s_waitcnt lgkmcnt(4)
	v_mfma_f32_32x32x16_bf16 v[20:35], v[96:99], v[80:83], v[20:35]
	s_waitcnt lgkmcnt(3)
	v_mfma_f32_32x32x16_bf16 v[4:19], v[100:103], v[68:71], v[4:19]
	s_waitcnt lgkmcnt(2)
	v_mfma_f32_32x32x16_bf16 v[4:19], v[104:107], v[72:75], v[4:19]
	s_waitcnt lgkmcnt(1)
	v_mfma_f32_32x32x16_bf16 v[4:19], v[108:111], v[76:79], v[4:19]
	s_waitcnt lgkmcnt(0)
	v_mfma_f32_32x32x16_bf16 v[4:19], v[112:115], v[80:83], v[4:19]
	v_mov_b32_e32 v230, v116

.LBB6_1249:
	v_cndmask_b32_e32 v101, v101, v188, vcc
	v_cndmask_b32_e64 v116, v100, 1.0, vcc
	v_mov_b32_e32 v240, v101
	v_pk_add_f32 v[98:99], v[98:99], v[240:241] op_sel_hi:[1,0] neg_lo:[0,1] neg_hi:[0,1]
	v_pk_add_f32 v[96:97], v[96:97], v[240:241] op_sel_hi:[1,0] neg_lo:[0,1] neg_hi:[0,1]
	v_pk_add_f32 v[94:95], v[94:95], v[240:241] op_sel_hi:[1,0] neg_lo:[0,1] neg_hi:[0,1]
	v_pk_add_f32 v[92:93], v[92:93], v[240:241] op_sel_hi:[1,0] neg_lo:[0,1] neg_hi:[0,1]
	v_pk_add_f32 v[90:91], v[90:91], v[240:241] op_sel_hi:[1,0] neg_lo:[0,1] neg_hi:[0,1]
	v_pk_add_f32 v[88:89], v[88:89], v[240:241] op_sel_hi:[1,0] neg_lo:[0,1] neg_hi:[0,1]
	v_pk_add_f32 v[86:87], v[86:87], v[240:241] op_sel_hi:[1,0] neg_lo:[0,1] neg_hi:[0,1]
	v_pk_add_f32 v[84:85], v[84:85], v[240:241] op_sel_hi:[1,0] neg_lo:[0,1] neg_hi:[0,1]
	v_sub_f32_e32 v100, v83, v101
	v_sub_f32_e32 v102, v82, v101
	v_sub_f32_e32 v103, v81, v101
	v_sub_f32_e32 v104, v80, v101
	v_sub_f32_e32 v105, v79, v101
	v_sub_f32_e32 v106, v78, v101
	v_sub_f32_e32 v107, v77, v101
	v_sub_f32_e32 v108, v76, v101
	v_sub_f32_e32 v83, v75, v101
	v_sub_f32_e32 v75, v74, v101
	v_sub_f32_e32 v74, v73, v101
	v_sub_f32_e32 v73, v72, v101
	v_sub_f32_e32 v72, v71, v101
	v_sub_f32_e32 v71, v70, v101
	v_sub_f32_e32 v70, v69, v101
	v_sub_f32_e32 v69, v68, v101
	v_exp_f32_e32 v68, v84
	v_exp_f32_e32 v76, v69
	v_exp_f32_e32 v69, v85
	v_exp_f32_e32 v77, v70
	v_exp_f32_e32 v70, v86
	v_exp_f32_e32 v78, v71
	v_exp_f32_e32 v71, v87
	v_exp_f32_e32 v79, v72
	v_exp_f32_e32 v72, v88
	v_exp_f32_e32 v80, v73
	v_exp_f32_e32 v73, v89
	v_exp_f32_e32 v81, v74
	v_exp_f32_e32 v74, v90
	v_exp_f32_e32 v82, v75
	v_exp_f32_e32 v75, v91
	v_exp_f32_e32 v83, v83
	v_exp_f32_e32 v84, v92
	v_exp_f32_e32 v86, v108
	v_exp_f32_e32 v85, v93
	v_exp_f32_e32 v87, v107
	v_exp_f32_e32 v88, v94
	v_exp_f32_e32 v90, v106
	v_exp_f32_e32 v89, v95
	v_exp_f32_e32 v91, v105
	v_exp_f32_e32 v92, v96
	v_exp_f32_e32 v94, v104
	v_exp_f32_e32 v93, v97
	v_exp_f32_e32 v95, v103
	v_exp_f32_e32 v96, v98
	v_exp_f32_e32 v98, v102
	v_exp_f32_e32 v97, v99
	v_exp_f32_e32 v99, v100
	v_pk_add_f32 v[100:101], v[90:91], v[88:89]
	v_pk_add_f32 v[102:103], v[78:79], v[70:71]
	v_pk_add_f32 v[106:107], v[82:83], v[74:75]
	v_pk_add_f32 v[104:105], v[98:99], v[96:97]
	v_pk_add_f32 v[108:109], v[86:87], v[84:85]
	v_pk_add_f32 v[110:111], v[76:77], v[68:69]
	v_pk_add_f32 v[112:113], v[94:95], v[92:93]
	v_pk_add_f32 v[114:115], v[80:81], v[72:73]
	v_pk_add_f32 v[108:109], v[110:111], v[108:109]
	v_pk_add_f32 v[112:113], v[114:115], v[112:113]
	v_pk_add_f32 v[104:105], v[106:107], v[104:105]
	v_pk_add_f32 v[100:101], v[102:103], v[100:101]
	v_pk_add_f32 v[102:103], v[108:109], v[112:113]
	v_pk_add_f32 v[100:101], v[100:101], v[104:105]
	v_cvt_pk_bf16_f32 v68, v68, v69
	v_pk_add_f32 v[100:101], v[102:103], v[100:101]
	v_cvt_pk_bf16_f32 v69, v70, v71
	v_cvt_pk_bf16_f32 v71, v74, v75
	v_cvt_pk_bf16_f32 v75, v96, v97
	v_add3_u32 v96, s1, v169, v2
	v_add3_u32 v2, s1, v2, v169
	v_add_f32_e32 v117, v100, v101
	v_cvt_pk_bf16_f32 v70, v72, v73
	v_cvt_pk_bf16_f32 v72, v84, v85
	v_cvt_pk_bf16_f32 v73, v88, v89
	v_cvt_pk_bf16_f32 v74, v92, v93
	v_cvt_pk_bf16_f32 v76, v76, v77
	v_cvt_pk_bf16_f32 v77, v78, v79
	v_cvt_pk_bf16_f32 v78, v80, v81
	v_cvt_pk_bf16_f32 v79, v82, v83
	v_cvt_pk_bf16_f32 v80, v86, v87
	v_cvt_pk_bf16_f32 v81, v90, v91
	v_cvt_pk_bf16_f32 v82, v94, v95
	v_cvt_pk_bf16_f32 v83, v98, v99
	ds_read_b128 v[84:87], v96 offset:25600
	ds_read_b128 v[88:91], v96 offset:25632
	ds_read_b128 v[92:95], v96 offset:25664
	ds_read_b128 v[96:99], v96 offset:25696
	ds_read_b128 v[100:103], v2 offset:30208
	ds_read_b128 v[104:107], v2 offset:30240
	ds_read_b128 v[108:111], v2 offset:30272
	ds_read_b128 v[112:115], v2 offset:30304
	v_fmac_f32_e32 v117, v187, v116
	s_waitcnt lgkmcnt(7)
	v_mfma_f32_32x32x16_bf16 v[52:67], v[84:87], v[68:71], v[52:67]
	s_waitcnt lgkmcnt(6)
	v_mfma_f32_32x32x16_bf16 v[52:67], v[88:91], v[72:75], v[52:67]
	s_waitcnt lgkmcnt(5)
	v_mfma_f32_32x32x16_bf16 v[52:67], v[92:95], v[76:79], v[52:67]
	s_waitcnt lgkmcnt(4)
	v_mfma_f32_32x32x16_bf16 v[52:67], v[96:99], v[80:83], v[52:67]
	ds_read_b128 v[84:87], v2 offset:34816
	ds_read_b128 v[88:91], v2 offset:34848
	ds_read_b128 v[92:95], v2 offset:34880
	ds_read_b128 v[96:99], v2 offset:34912
	s_waitcnt lgkmcnt(7)
	v_mfma_f32_32x32x16_bf16 v[36:51], v[100:103], v[68:71], v[36:51]
	s_waitcnt lgkmcnt(6)
	v_mfma_f32_32x32x16_bf16 v[36:51], v[104:107], v[72:75], v[36:51]
	s_waitcnt lgkmcnt(5)
	v_mfma_f32_32x32x16_bf16 v[36:51], v[108:111], v[76:79], v[36:51]
	s_waitcnt lgkmcnt(4)
	v_mfma_f32_32x32x16_bf16 v[36:51], v[112:115], v[80:83], v[36:51]
	ds_read_b128 v[100:103], v2 offset:39424
	ds_read_b128 v[104:107], v2 offset:39456
	ds_read_b128 v[108:111], v2 offset:39488
	ds_read_b128 v[112:115], v2 offset:39520
	s_waitcnt lgkmcnt(7)
	v_mfma_f32_32x32x16_bf16 v[20:35], v[84:87], v[68:71], v[20:35]
	s_waitcnt lgkmcnt(6)
	v_mfma_f32_32x32x16_bf16 v[20:35], v[88:91], v[72:75], v[20:35]
	s_waitcnt lgkmcnt(5)
	v_mfma_f32_32x32x16_bf16 v[20:35], v[92:95], v[76:79], v[20:35]
	s_waitcnt lgkmcnt(4)
	v_mfma_f32_32x32x16_bf16 v[20:35], v[96:99], v[80:83], v[20:35]
	s_waitcnt lgkmcnt(3)
	v_mfma_f32_32x32x16_bf16 v[4:19], v[100:103], v[68:71], v[4:19]
	s_waitcnt lgkmcnt(2)
	v_mfma_f32_32x32x16_bf16 v[4:19], v[104:107], v[72:75], v[4:19]
	s_waitcnt lgkmcnt(1)
	v_mfma_f32_32x32x16_bf16 v[4:19], v[108:111], v[76:79], v[4:19]
	s_waitcnt lgkmcnt(0)
	v_mfma_f32_32x32x16_bf16 v[4:19], v[112:115], v[80:83], v[4:19]
	v_mov_b32_e32 v187, v117

.LBB6_1259:
	s_nop 8
	s_nop 4
	s_nop 0
	v_max_f32_e32 v152, v91, v75
	v_max_f32_e32 v140, v88, v72
	v_max_f32_e32 v150, v89, v73
	v_max_f32_e32 v151, v90, v74
	v_max3_f32 v152, v87, v71, v152
	v_max3_f32 v140, v84, v68, v140
	v_max3_f32 v150, v85, v69, v150
	v_max3_f32 v151, v86, v70, v151
	v_max3_f32 v152, v95, v79, v152
	v_max3_f32 v140, v92, v76, v140
	v_max3_f32 v150, v93, v77, v150
	v_max3_f32 v151, v94, v78, v151
	v_max_f32_e32 v153, v98, v82
	v_max3_f32 v152, v99, v83, v152
	v_max3_f32 v140, v96, v80, v140
	v_max3_f32 v150, v97, v81, v150
	v_max3_f32 v151, v153, v151, v152
	v_max3_f32 v140, v140, v150, v151
	v_mov_b32_e32 v150, v140
	s_nop 1
	v_permlane32_swap_b32_e32 v140, v150
	v_max_f32_e32 v150, v150, v150
	v_max_f32_e32 v140, v140, v140
	v_max_f32_e32 v140, v140, v150
	v_mul_f32_e32 v140, s42, v140
	v_sub_f32_e32 v150, v140, v131
	v_cmp_ge_f32_e32 vcc, s97, v150
	v_max_f32_e32 v150, v131, v131
	v_max_f32_e32 v150, v150, v140
	v_sub_f32_e32 v140, v131, v150
	v_exp_f32_e32 v140, v140
	s_cmp_eq_u64 vcc, exec
	s_cselect_b64 vcc, -1, 0
	s_cbranch_vccnz .LBB6_1261
	v_pk_mul_f32 v[66:67], v[66:67], v[140:141] op_sel_hi:[1,0]
	v_pk_mul_f32 v[64:65], v[64:65], v[140:141] op_sel_hi:[1,0]
	v_pk_mul_f32 v[62:63], v[62:63], v[140:141] op_sel_hi:[1,0]
	v_pk_mul_f32 v[60:61], v[60:61], v[140:141] op_sel_hi:[1,0]
	v_pk_mul_f32 v[58:59], v[58:59], v[140:141] op_sel_hi:[1,0]
	v_pk_mul_f32 v[56:57], v[56:57], v[140:141] op_sel_hi:[1,0]
	v_pk_mul_f32 v[54:55], v[54:55], v[140:141] op_sel_hi:[1,0]
	v_pk_mul_f32 v[52:53], v[52:53], v[140:141] op_sel_hi:[1,0]
	v_pk_mul_f32 v[50:51], v[50:51], v[140:141] op_sel_hi:[1,0]
	v_pk_mul_f32 v[48:49], v[48:49], v[140:141] op_sel_hi:[1,0]
	v_pk_mul_f32 v[46:47], v[46:47], v[140:141] op_sel_hi:[1,0]
	v_pk_mul_f32 v[44:45], v[44:45], v[140:141] op_sel_hi:[1,0]
	v_pk_mul_f32 v[42:43], v[42:43], v[140:141] op_sel_hi:[1,0]
	v_pk_mul_f32 v[40:41], v[40:41], v[140:141] op_sel_hi:[1,0]
	v_pk_mul_f32 v[38:39], v[38:39], v[140:141] op_sel_hi:[1,0]
	v_pk_mul_f32 v[36:37], v[36:37], v[140:141] op_sel_hi:[1,0]
	v_pk_mul_f32 v[34:35], v[34:35], v[140:141] op_sel_hi:[1,0]
	v_pk_mul_f32 v[32:33], v[32:33], v[140:141] op_sel_hi:[1,0]
	v_pk_mul_f32 v[30:31], v[30:31], v[140:141] op_sel_hi:[1,0]
	v_pk_mul_f32 v[28:29], v[28:29], v[140:141] op_sel_hi:[1,0]
	v_pk_mul_f32 v[26:27], v[26:27], v[140:141] op_sel_hi:[1,0]
	v_pk_mul_f32 v[24:25], v[24:25], v[140:141] op_sel_hi:[1,0]
	v_pk_mul_f32 v[22:23], v[22:23], v[140:141] op_sel_hi:[1,0]
	v_pk_mul_f32 v[20:21], v[20:21], v[140:141] op_sel_hi:[1,0]
	v_pk_mul_f32 v[18:19], v[18:19], v[140:141] op_sel_hi:[1,0]
	v_pk_mul_f32 v[16:17], v[16:17], v[140:141] op_sel_hi:[1,0]
	v_pk_mul_f32 v[14:15], v[14:15], v[140:141] op_sel_hi:[1,0]
	v_pk_mul_f32 v[12:13], v[12:13], v[140:141] op_sel_hi:[1,0]
	v_pk_mul_f32 v[10:11], v[10:11], v[140:141] op_sel_hi:[1,0]
	v_pk_mul_f32 v[8:9], v[8:9], v[140:141] op_sel_hi:[1,0]
	v_pk_mul_f32 v[6:7], v[6:7], v[140:141] op_sel_hi:[1,0]
	v_pk_mul_f32 v[4:5], v[4:5], v[140:141] op_sel_hi:[1,0]
.LBB6_1261:
	v_cndmask_b32_e32 v131, v150, v131, vcc
	v_mov_b32_e32 v238, v131
	v_pk_fma_f32 v[98:99], v[98:99], s[42:43], v[238:239] op_sel_hi:[1,0,0] neg_lo:[0,0,1] neg_hi:[0,0,1]
	v_pk_fma_f32 v[96:97], v[96:97], s[42:43], v[238:239] op_sel_hi:[1,0,0] neg_lo:[0,0,1] neg_hi:[0,0,1]
	v_pk_fma_f32 v[94:95], v[94:95], s[42:43], v[238:239] op_sel_hi:[1,0,0] neg_lo:[0,0,1] neg_hi:[0,0,1]
	v_pk_fma_f32 v[92:93], v[92:93], s[42:43], v[238:239] op_sel_hi:[1,0,0] neg_lo:[0,0,1] neg_hi:[0,0,1]
	v_pk_fma_f32 v[90:91], v[90:91], s[42:43], v[238:239] op_sel_hi:[1,0,0] neg_lo:[0,0,1] neg_hi:[0,0,1]
	v_pk_fma_f32 v[88:89], v[88:89], s[42:43], v[238:239] op_sel_hi:[1,0,0] neg_lo:[0,0,1] neg_hi:[0,0,1]
	v_pk_fma_f32 v[86:87], v[86:87], s[42:43], v[238:239] op_sel_hi:[1,0,0] neg_lo:[0,0,1] neg_hi:[0,0,1]
	v_pk_fma_f32 v[84:85], v[84:85], s[42:43], v[238:239] op_sel_hi:[1,0,0] neg_lo:[0,0,1] neg_hi:[0,0,1]
	v_pk_fma_f32 v[216:217], v[82:83], s[42:43], v[238:239] op_sel_hi:[1,0,0] neg_lo:[0,0,1] neg_hi:[0,0,1]
	v_pk_fma_f32 v[218:219], v[80:81], s[42:43], v[238:239] op_sel_hi:[1,0,0] neg_lo:[0,0,1] neg_hi:[0,0,1]
	v_pk_fma_f32 v[220:221], v[78:79], s[42:43], v[238:239] op_sel_hi:[1,0,0] neg_lo:[0,0,1] neg_hi:[0,0,1]
	v_pk_fma_f32 v[222:223], v[76:77], s[42:43], v[238:239] op_sel_hi:[1,0,0] neg_lo:[0,0,1] neg_hi:[0,0,1]
	v_pk_fma_f32 v[230:231], v[68:69], s[42:43], v[238:239] op_sel_hi:[1,0,0] neg_lo:[0,0,1] neg_hi:[0,0,1]
	v_pk_fma_f32 v[232:233], v[70:71], s[42:43], v[238:239] op_sel_hi:[1,0,0] neg_lo:[0,0,1] neg_hi:[0,0,1]
	v_pk_fma_f32 v[234:235], v[72:73], s[42:43], v[238:239] op_sel_hi:[1,0,0] neg_lo:[0,0,1] neg_hi:[0,0,1]
	v_pk_fma_f32 v[236:237], v[74:75], s[42:43], v[238:239] op_sel_hi:[1,0,0] neg_lo:[0,0,1] neg_hi:[0,0,1]
	v_exp_f32_e32 v68, v84
	v_exp_f32_e32 v76, v230
	v_exp_f32_e32 v69, v85
	v_exp_f32_e32 v77, v231
	v_exp_f32_e32 v70, v86
	v_exp_f32_e32 v78, v232
	v_exp_f32_e32 v71, v87
	v_exp_f32_e32 v79, v233
	v_exp_f32_e32 v72, v88
	v_exp_f32_e32 v80, v234
	v_exp_f32_e32 v73, v89
	v_exp_f32_e32 v81, v235
	v_exp_f32_e32 v74, v90
	v_exp_f32_e32 v82, v236
	v_exp_f32_e32 v75, v91
	v_exp_f32_e32 v83, v237
	v_exp_f32_e32 v84, v92
	v_exp_f32_e32 v86, v222
	v_exp_f32_e32 v85, v93
	v_exp_f32_e32 v87, v223
	v_exp_f32_e32 v88, v94
	v_exp_f32_e32 v90, v220
	v_exp_f32_e32 v89, v95
	v_exp_f32_e32 v91, v221
	v_exp_f32_e32 v92, v96
	v_exp_f32_e32 v94, v218
	v_exp_f32_e32 v93, v97
	v_exp_f32_e32 v95, v219
	v_exp_f32_e32 v96, v98
	v_exp_f32_e32 v98, v216
	v_exp_f32_e32 v97, v99
	v_exp_f32_e32 v99, v217
	v_pk_add_f32 v[150:151], v[90:91], v[88:89]
	v_pk_add_f32 v[152:153], v[78:79], v[70:71]
	v_pk_add_f32 v[156:157], v[82:83], v[74:75]
	v_pk_add_f32 v[154:155], v[98:99], v[96:97]
	v_pk_add_f32 v[158:159], v[86:87], v[84:85]
	v_pk_add_f32 v[160:161], v[76:77], v[68:69]
	v_pk_add_f32 v[162:163], v[94:95], v[92:93]
	v_pk_add_f32 v[164:165], v[80:81], v[72:73]
	v_pk_add_f32 v[158:159], v[160:161], v[158:159]
	v_pk_add_f32 v[162:163], v[164:165], v[162:163]
	v_pk_add_f32 v[154:155], v[156:157], v[154:155]
	v_pk_add_f32 v[150:151], v[152:153], v[150:151]
	v_pk_add_f32 v[152:153], v[158:159], v[162:163]
	v_pk_add_f32 v[150:151], v[150:151], v[154:155]
	v_cndmask_b32_e64 v140, v140, 1.0, vcc
	v_pk_add_f32 v[150:151], v[152:153], v[150:151]
	v_cvt_pk_bf16_f32 v68, v68, v69
	v_add_f32_e32 v166, v150, v151
	v_fmac_f32_e32 v166, v141, v140
	v_cvt_pk_bf16_f32 v69, v70, v71
	v_cvt_pk_bf16_f32 v71, v74, v75
	v_cvt_pk_bf16_f32 v75, v96, v97
	v_add3_u32 v96, s49, v129, v2
	v_add3_u32 v140, s49, v2, v129
	v_cvt_pk_bf16_f32 v70, v72, v73
	v_cvt_pk_bf16_f32 v72, v84, v85
	v_cvt_pk_bf16_f32 v73, v88, v89
	v_cvt_pk_bf16_f32 v74, v92, v93
	v_cvt_pk_bf16_f32 v76, v76, v77
	v_cvt_pk_bf16_f32 v77, v78, v79
	v_cvt_pk_bf16_f32 v78, v80, v81
	v_cvt_pk_bf16_f32 v79, v82, v83
	v_cvt_pk_bf16_f32 v80, v86, v87
	v_cvt_pk_bf16_f32 v81, v90, v91
	v_cvt_pk_bf16_f32 v82, v94, v95
	v_cvt_pk_bf16_f32 v83, v98, v99
	ds_read_b128 v[84:87], v96 offset:9216
	ds_read_b128 v[88:91], v96 offset:9248
	ds_read_b128 v[92:95], v96 offset:9280
	ds_read_b128 v[96:99], v96 offset:9312
	ds_read_b128 v[150:153], v140 offset:13824
	ds_read_b128 v[154:157], v140 offset:13856
	ds_read_b128 v[158:161], v140 offset:13888
	ds_read_b128 v[162:165], v140 offset:13920
	s_waitcnt lgkmcnt(7)
	v_mfma_f32_32x32x16_bf16 v[52:67], v[84:87], v[68:71], v[52:67]
	s_waitcnt lgkmcnt(6)
	v_mfma_f32_32x32x16_bf16 v[52:67], v[88:91], v[72:75], v[52:67]
	s_waitcnt lgkmcnt(5)
	v_mfma_f32_32x32x16_bf16 v[52:67], v[92:95], v[76:79], v[52:67]
	s_waitcnt lgkmcnt(4)
	v_mfma_f32_32x32x16_bf16 v[52:67], v[96:99], v[80:83], v[52:67]
	ds_read_b128 v[84:87], v140 offset:18432
	ds_read_b128 v[88:91], v140 offset:18464
	ds_read_b128 v[92:95], v140 offset:18496
	ds_read_b128 v[96:99], v140 offset:18528
	s_waitcnt lgkmcnt(7)
	v_mfma_f32_32x32x16_bf16 v[36:51], v[150:153], v[68:71], v[36:51]
	s_waitcnt lgkmcnt(6)
	v_mfma_f32_32x32x16_bf16 v[36:51], v[154:157], v[72:75], v[36:51]
	s_waitcnt lgkmcnt(5)
	v_mfma_f32_32x32x16_bf16 v[36:51], v[158:161], v[76:79], v[36:51]
	s_waitcnt lgkmcnt(4)
	v_mfma_f32_32x32x16_bf16 v[36:51], v[162:165], v[80:83], v[36:51]
	ds_read_b128 v[150:153], v140 offset:23040
	ds_read_b128 v[154:157], v140 offset:23072
	ds_read_b128 v[158:161], v140 offset:23104
	ds_read_b128 v[162:165], v140 offset:23136
	s_waitcnt lgkmcnt(7)
	v_mfma_f32_32x32x16_bf16 v[20:35], v[84:87], v[68:71], v[20:35]
	s_waitcnt lgkmcnt(6)
	v_mfma_f32_32x32x16_bf16 v[20:35], v[88:91], v[72:75], v[20:35]
	s_waitcnt lgkmcnt(5)
	v_mfma_f32_32x32x16_bf16 v[20:35], v[92:95], v[76:79], v[20:35]
	s_waitcnt lgkmcnt(4)
	v_mfma_f32_32x32x16_bf16 v[20:35], v[96:99], v[80:83], v[20:35]
	s_waitcnt lgkmcnt(3)
	v_mfma_f32_32x32x16_bf16 v[4:19], v[150:153], v[68:71], v[4:19]
	s_waitcnt lgkmcnt(2)
	v_mfma_f32_32x32x16_bf16 v[4:19], v[154:157], v[72:75], v[4:19]
	s_waitcnt lgkmcnt(1)
	v_mfma_f32_32x32x16_bf16 v[4:19], v[158:161], v[76:79], v[4:19]
	s_waitcnt lgkmcnt(0)
	v_mfma_f32_32x32x16_bf16 v[4:19], v[162:165], v[80:83], v[4:19]
	v_mov_b32_e32 v141, v166

.LBB6_1267:
	s_nop 8
	s_nop 4
	s_nop 0
	v_max_f32_e32 v103, v91, v75
	v_max_f32_e32 v100, v88, v72
	v_max_f32_e32 v101, v89, v73
	v_max_f32_e32 v102, v90, v74
	v_max3_f32 v103, v87, v71, v103
	v_max3_f32 v100, v84, v68, v100
	v_max3_f32 v101, v85, v69, v101
	v_max3_f32 v102, v86, v70, v102
	v_max3_f32 v103, v95, v79, v103
	v_max3_f32 v100, v92, v76, v100
	v_max3_f32 v101, v93, v77, v101
	v_max3_f32 v102, v94, v78, v102
	v_max_f32_e32 v104, v98, v82
	v_max3_f32 v103, v99, v83, v103
	v_max3_f32 v100, v96, v80, v100
	v_max3_f32 v101, v97, v81, v101
	v_max3_f32 v102, v104, v102, v103
	v_max3_f32 v100, v100, v101, v102
	v_mov_b32_e32 v101, v100
	s_nop 1
	v_permlane32_swap_b32_e32 v100, v101
	v_max_f32_e32 v101, v101, v101
	v_max_f32_e32 v100, v100, v100
	v_max_f32_e32 v100, v100, v101
	v_mul_f32_e32 v100, s42, v100
	v_sub_f32_e32 v101, v100, v131
	v_cmp_ge_f32_e32 vcc, s97, v101
	v_max_f32_e32 v101, v131, v131
	v_max_f32_e32 v101, v101, v100
	v_sub_f32_e32 v100, v131, v101
	v_exp_f32_e32 v100, v100
	s_cmp_eq_u64 vcc, exec
	s_cselect_b64 vcc, -1, 0
	s_cbranch_vccnz .LBB6_1269
	v_pk_mul_f32 v[66:67], v[66:67], v[100:101] op_sel_hi:[1,0]
	v_pk_mul_f32 v[64:65], v[64:65], v[100:101] op_sel_hi:[1,0]
	v_pk_mul_f32 v[62:63], v[62:63], v[100:101] op_sel_hi:[1,0]
	v_pk_mul_f32 v[60:61], v[60:61], v[100:101] op_sel_hi:[1,0]
	v_pk_mul_f32 v[58:59], v[58:59], v[100:101] op_sel_hi:[1,0]
	v_pk_mul_f32 v[56:57], v[56:57], v[100:101] op_sel_hi:[1,0]
	v_pk_mul_f32 v[54:55], v[54:55], v[100:101] op_sel_hi:[1,0]
	v_pk_mul_f32 v[52:53], v[52:53], v[100:101] op_sel_hi:[1,0]
	v_pk_mul_f32 v[50:51], v[50:51], v[100:101] op_sel_hi:[1,0]
	v_pk_mul_f32 v[48:49], v[48:49], v[100:101] op_sel_hi:[1,0]
	v_pk_mul_f32 v[46:47], v[46:47], v[100:101] op_sel_hi:[1,0]
	v_pk_mul_f32 v[44:45], v[44:45], v[100:101] op_sel_hi:[1,0]
	v_pk_mul_f32 v[42:43], v[42:43], v[100:101] op_sel_hi:[1,0]
	v_pk_mul_f32 v[40:41], v[40:41], v[100:101] op_sel_hi:[1,0]
	v_pk_mul_f32 v[38:39], v[38:39], v[100:101] op_sel_hi:[1,0]
	v_pk_mul_f32 v[36:37], v[36:37], v[100:101] op_sel_hi:[1,0]
	v_pk_mul_f32 v[34:35], v[34:35], v[100:101] op_sel_hi:[1,0]
	v_pk_mul_f32 v[32:33], v[32:33], v[100:101] op_sel_hi:[1,0]
	v_pk_mul_f32 v[30:31], v[30:31], v[100:101] op_sel_hi:[1,0]
	v_pk_mul_f32 v[28:29], v[28:29], v[100:101] op_sel_hi:[1,0]
	v_pk_mul_f32 v[26:27], v[26:27], v[100:101] op_sel_hi:[1,0]
	v_pk_mul_f32 v[24:25], v[24:25], v[100:101] op_sel_hi:[1,0]
	v_pk_mul_f32 v[22:23], v[22:23], v[100:101] op_sel_hi:[1,0]
	v_pk_mul_f32 v[20:21], v[20:21], v[100:101] op_sel_hi:[1,0]
	v_pk_mul_f32 v[18:19], v[18:19], v[100:101] op_sel_hi:[1,0]
	v_pk_mul_f32 v[16:17], v[16:17], v[100:101] op_sel_hi:[1,0]
	v_pk_mul_f32 v[14:15], v[14:15], v[100:101] op_sel_hi:[1,0]
	v_pk_mul_f32 v[12:13], v[12:13], v[100:101] op_sel_hi:[1,0]
	v_pk_mul_f32 v[10:11], v[10:11], v[100:101] op_sel_hi:[1,0]
	v_pk_mul_f32 v[8:9], v[8:9], v[100:101] op_sel_hi:[1,0]
	v_pk_mul_f32 v[6:7], v[6:7], v[100:101] op_sel_hi:[1,0]
	v_pk_mul_f32 v[4:5], v[4:5], v[100:101] op_sel_hi:[1,0]
.LBB6_1269:
	v_cndmask_b32_e32 v101, v101, v131, vcc
	v_cndmask_b32_e64 v116, v100, 1.0, vcc
	v_mov_b32_e32 v238, v101
	v_pk_fma_f32 v[98:99], v[98:99], s[42:43], v[238:239] op_sel_hi:[1,0,0] neg_lo:[0,0,1] neg_hi:[0,0,1]
	v_pk_fma_f32 v[96:97], v[96:97], s[42:43], v[238:239] op_sel_hi:[1,0,0] neg_lo:[0,0,1] neg_hi:[0,0,1]
	v_pk_fma_f32 v[94:95], v[94:95], s[42:43], v[238:239] op_sel_hi:[1,0,0] neg_lo:[0,0,1] neg_hi:[0,0,1]
	v_pk_fma_f32 v[92:93], v[92:93], s[42:43], v[238:239] op_sel_hi:[1,0,0] neg_lo:[0,0,1] neg_hi:[0,0,1]
	v_pk_fma_f32 v[90:91], v[90:91], s[42:43], v[238:239] op_sel_hi:[1,0,0] neg_lo:[0,0,1] neg_hi:[0,0,1]
	v_pk_fma_f32 v[88:89], v[88:89], s[42:43], v[238:239] op_sel_hi:[1,0,0] neg_lo:[0,0,1] neg_hi:[0,0,1]
	v_pk_fma_f32 v[86:87], v[86:87], s[42:43], v[238:239] op_sel_hi:[1,0,0] neg_lo:[0,0,1] neg_hi:[0,0,1]
	v_pk_fma_f32 v[84:85], v[84:85], s[42:43], v[238:239] op_sel_hi:[1,0,0] neg_lo:[0,0,1] neg_hi:[0,0,1]
	v_pk_fma_f32 v[216:217], v[82:83], s[42:43], v[238:239] op_sel_hi:[1,0,0] neg_lo:[0,0,1] neg_hi:[0,0,1]
	v_pk_fma_f32 v[218:219], v[80:81], s[42:43], v[238:239] op_sel_hi:[1,0,0] neg_lo:[0,0,1] neg_hi:[0,0,1]
	v_pk_fma_f32 v[220:221], v[78:79], s[42:43], v[238:239] op_sel_hi:[1,0,0] neg_lo:[0,0,1] neg_hi:[0,0,1]
	v_pk_fma_f32 v[222:223], v[76:77], s[42:43], v[238:239] op_sel_hi:[1,0,0] neg_lo:[0,0,1] neg_hi:[0,0,1]
	v_pk_fma_f32 v[230:231], v[68:69], s[42:43], v[238:239] op_sel_hi:[1,0,0] neg_lo:[0,0,1] neg_hi:[0,0,1]
	v_pk_fma_f32 v[232:233], v[70:71], s[42:43], v[238:239] op_sel_hi:[1,0,0] neg_lo:[0,0,1] neg_hi:[0,0,1]
	v_pk_fma_f32 v[234:235], v[72:73], s[42:43], v[238:239] op_sel_hi:[1,0,0] neg_lo:[0,0,1] neg_hi:[0,0,1]
	v_pk_fma_f32 v[236:237], v[74:75], s[42:43], v[238:239] op_sel_hi:[1,0,0] neg_lo:[0,0,1] neg_hi:[0,0,1]
	v_exp_f32_e32 v68, v84
	v_exp_f32_e32 v76, v230
	v_exp_f32_e32 v69, v85
	v_exp_f32_e32 v77, v231
	v_exp_f32_e32 v70, v86
	v_exp_f32_e32 v78, v232
	v_exp_f32_e32 v71, v87
	v_exp_f32_e32 v79, v233
	v_exp_f32_e32 v72, v88
	v_exp_f32_e32 v80, v234
	v_exp_f32_e32 v73, v89
	v_exp_f32_e32 v81, v235
	v_exp_f32_e32 v74, v90
	v_exp_f32_e32 v82, v236
	v_exp_f32_e32 v75, v91
	v_exp_f32_e32 v83, v237
	v_exp_f32_e32 v84, v92
	v_exp_f32_e32 v86, v222
	v_exp_f32_e32 v85, v93
	v_exp_f32_e32 v87, v223
	v_exp_f32_e32 v88, v94
	v_exp_f32_e32 v90, v220
	v_exp_f32_e32 v89, v95
	v_exp_f32_e32 v91, v221
	v_exp_f32_e32 v92, v96
	v_exp_f32_e32 v94, v218
	v_exp_f32_e32 v93, v97
	v_exp_f32_e32 v95, v219
	v_exp_f32_e32 v96, v98
	v_exp_f32_e32 v98, v216
	v_exp_f32_e32 v97, v99
	v_exp_f32_e32 v99, v217
	v_pk_add_f32 v[100:101], v[90:91], v[88:89]
	v_pk_add_f32 v[102:103], v[78:79], v[70:71]
	v_pk_add_f32 v[106:107], v[82:83], v[74:75]
	v_pk_add_f32 v[104:105], v[98:99], v[96:97]
	v_pk_add_f32 v[108:109], v[86:87], v[84:85]
	v_pk_add_f32 v[110:111], v[76:77], v[68:69]
	v_pk_add_f32 v[112:113], v[94:95], v[92:93]
	v_pk_add_f32 v[114:115], v[80:81], v[72:73]
	v_pk_add_f32 v[108:109], v[110:111], v[108:109]
	v_pk_add_f32 v[112:113], v[114:115], v[112:113]
	v_pk_add_f32 v[104:105], v[106:107], v[104:105]
	v_pk_add_f32 v[100:101], v[102:103], v[100:101]
	v_pk_add_f32 v[102:103], v[108:109], v[112:113]
	v_pk_add_f32 v[100:101], v[100:101], v[104:105]
	v_cvt_pk_bf16_f32 v68, v68, v69
	v_pk_add_f32 v[100:101], v[102:103], v[100:101]
	v_cvt_pk_bf16_f32 v69, v70, v71
	v_cvt_pk_bf16_f32 v71, v74, v75
	v_cvt_pk_bf16_f32 v75, v96, v97
	v_add3_u32 v96, s12, v129, v2
	v_add3_u32 v2, s12, v2, v129
	v_add_f32_e32 v117, v100, v101
	v_cvt_pk_bf16_f32 v70, v72, v73
	v_cvt_pk_bf16_f32 v72, v84, v85
	v_cvt_pk_bf16_f32 v73, v88, v89
	v_cvt_pk_bf16_f32 v74, v92, v93
	v_cvt_pk_bf16_f32 v76, v76, v77
	v_cvt_pk_bf16_f32 v77, v78, v79
	v_cvt_pk_bf16_f32 v78, v80, v81
	v_cvt_pk_bf16_f32 v79, v82, v83
	v_cvt_pk_bf16_f32 v80, v86, v87
	v_cvt_pk_bf16_f32 v81, v90, v91
	v_cvt_pk_bf16_f32 v82, v94, v95
	v_cvt_pk_bf16_f32 v83, v98, v99
	ds_read_b128 v[84:87], v96 offset:9216
	ds_read_b128 v[88:91], v96 offset:9248
	ds_read_b128 v[92:95], v96 offset:9280
	ds_read_b128 v[96:99], v96 offset:9312
	ds_read_b128 v[100:103], v2 offset:13824
	ds_read_b128 v[104:107], v2 offset:13856
	ds_read_b128 v[108:111], v2 offset:13888
	ds_read_b128 v[112:115], v2 offset:13920
	v_fmac_f32_e32 v117, v141, v116
	s_waitcnt lgkmcnt(7)
	v_mfma_f32_32x32x16_bf16 v[52:67], v[84:87], v[68:71], v[52:67]
	s_waitcnt lgkmcnt(6)
	v_mfma_f32_32x32x16_bf16 v[52:67], v[88:91], v[72:75], v[52:67]
	s_waitcnt lgkmcnt(5)
	v_mfma_f32_32x32x16_bf16 v[52:67], v[92:95], v[76:79], v[52:67]
	s_waitcnt lgkmcnt(4)
	v_mfma_f32_32x32x16_bf16 v[52:67], v[96:99], v[80:83], v[52:67]
	ds_read_b128 v[84:87], v2 offset:18432
	ds_read_b128 v[88:91], v2 offset:18464
	ds_read_b128 v[92:95], v2 offset:18496
	ds_read_b128 v[96:99], v2 offset:18528
	s_waitcnt lgkmcnt(7)
	v_mfma_f32_32x32x16_bf16 v[36:51], v[100:103], v[68:71], v[36:51]
	s_waitcnt lgkmcnt(6)
	v_mfma_f32_32x32x16_bf16 v[36:51], v[104:107], v[72:75], v[36:51]
	s_waitcnt lgkmcnt(5)
	v_mfma_f32_32x32x16_bf16 v[36:51], v[108:111], v[76:79], v[36:51]
	s_waitcnt lgkmcnt(4)
	v_mfma_f32_32x32x16_bf16 v[36:51], v[112:115], v[80:83], v[36:51]
	ds_read_b128 v[100:103], v2 offset:23040
	ds_read_b128 v[104:107], v2 offset:23072
	ds_read_b128 v[108:111], v2 offset:23104
	ds_read_b128 v[112:115], v2 offset:23136
	s_waitcnt lgkmcnt(7)
	v_mfma_f32_32x32x16_bf16 v[20:35], v[84:87], v[68:71], v[20:35]
	s_waitcnt lgkmcnt(6)
	v_mfma_f32_32x32x16_bf16 v[20:35], v[88:91], v[72:75], v[20:35]
	s_waitcnt lgkmcnt(5)
	v_mfma_f32_32x32x16_bf16 v[20:35], v[92:95], v[76:79], v[20:35]
	s_waitcnt lgkmcnt(4)
	v_mfma_f32_32x32x16_bf16 v[20:35], v[96:99], v[80:83], v[20:35]
	s_waitcnt lgkmcnt(3)
	v_mfma_f32_32x32x16_bf16 v[4:19], v[100:103], v[68:71], v[4:19]
	s_waitcnt lgkmcnt(2)
	v_mfma_f32_32x32x16_bf16 v[4:19], v[104:107], v[72:75], v[4:19]
	s_waitcnt lgkmcnt(1)
	v_mfma_f32_32x32x16_bf16 v[4:19], v[108:111], v[76:79], v[4:19]
	s_waitcnt lgkmcnt(0)
	v_mfma_f32_32x32x16_bf16 v[4:19], v[112:115], v[80:83], v[4:19]
	v_mov_b32_e32 v141, v117

.LBB6_1276:
	s_nop 8
	s_nop 4
	s_nop 0
	v_max_f32_e32 v156, v91, v75
	v_max_f32_e32 v144, v88, v72
	v_max_f32_e32 v154, v89, v73
	v_max_f32_e32 v155, v90, v74
	v_max3_f32 v156, v87, v71, v156
	v_max3_f32 v144, v84, v68, v144
	v_max3_f32 v154, v85, v69, v154
	v_max3_f32 v155, v86, v70, v155
	v_max3_f32 v156, v95, v79, v156
	v_max3_f32 v144, v92, v76, v144
	v_max3_f32 v154, v93, v77, v154
	v_max3_f32 v155, v94, v78, v155
	v_max_f32_e32 v157, v98, v82
	v_max3_f32 v156, v99, v83, v156
	v_max3_f32 v144, v96, v80, v144
	v_max3_f32 v154, v97, v81, v154
	v_max3_f32 v155, v157, v155, v156
	v_max3_f32 v144, v144, v154, v155
	v_mov_b32_e32 v154, v144
	s_nop 1
	v_permlane32_swap_b32_e32 v144, v154
	v_max_f32_e32 v154, v154, v154
	v_max_f32_e32 v144, v144, v144
	v_max_f32_e32 v144, v144, v154
	v_mul_f32_e32 v144, s42, v144
	v_sub_f32_e32 v154, v144, v135
	v_cmp_ge_f32_e32 vcc, s97, v154
	v_max_f32_e32 v154, v135, v135
	v_max_f32_e32 v154, v154, v144
	v_sub_f32_e32 v144, v135, v154
	v_exp_f32_e32 v144, v144
	s_cmp_eq_u64 vcc, exec
	s_cselect_b64 vcc, -1, 0
	s_cbranch_vccnz .LBB6_1278
	v_pk_mul_f32 v[18:19], v[18:19], v[144:145] op_sel_hi:[1,0]
	v_pk_mul_f32 v[16:17], v[16:17], v[144:145] op_sel_hi:[1,0]
	v_pk_mul_f32 v[14:15], v[14:15], v[144:145] op_sel_hi:[1,0]
	v_pk_mul_f32 v[12:13], v[12:13], v[144:145] op_sel_hi:[1,0]
	v_pk_mul_f32 v[10:11], v[10:11], v[144:145] op_sel_hi:[1,0]
	v_pk_mul_f32 v[8:9], v[8:9], v[144:145] op_sel_hi:[1,0]
	v_pk_mul_f32 v[6:7], v[6:7], v[144:145] op_sel_hi:[1,0]
	v_pk_mul_f32 v[4:5], v[4:5], v[144:145] op_sel_hi:[1,0]
	v_pk_mul_f32 v[66:67], v[66:67], v[144:145] op_sel_hi:[1,0]
	v_pk_mul_f32 v[64:65], v[64:65], v[144:145] op_sel_hi:[1,0]
	v_pk_mul_f32 v[62:63], v[62:63], v[144:145] op_sel_hi:[1,0]
	v_pk_mul_f32 v[60:61], v[60:61], v[144:145] op_sel_hi:[1,0]
	v_pk_mul_f32 v[58:59], v[58:59], v[144:145] op_sel_hi:[1,0]
	v_pk_mul_f32 v[56:57], v[56:57], v[144:145] op_sel_hi:[1,0]
	v_pk_mul_f32 v[54:55], v[54:55], v[144:145] op_sel_hi:[1,0]
	v_pk_mul_f32 v[52:53], v[52:53], v[144:145] op_sel_hi:[1,0]
	v_pk_mul_f32 v[50:51], v[50:51], v[144:145] op_sel_hi:[1,0]
	v_pk_mul_f32 v[48:49], v[48:49], v[144:145] op_sel_hi:[1,0]
	v_pk_mul_f32 v[46:47], v[46:47], v[144:145] op_sel_hi:[1,0]
	v_pk_mul_f32 v[44:45], v[44:45], v[144:145] op_sel_hi:[1,0]
	v_pk_mul_f32 v[42:43], v[42:43], v[144:145] op_sel_hi:[1,0]
	v_pk_mul_f32 v[40:41], v[40:41], v[144:145] op_sel_hi:[1,0]
	v_pk_mul_f32 v[38:39], v[38:39], v[144:145] op_sel_hi:[1,0]
	v_pk_mul_f32 v[36:37], v[36:37], v[144:145] op_sel_hi:[1,0]
	v_pk_mul_f32 v[34:35], v[34:35], v[144:145] op_sel_hi:[1,0]
	v_pk_mul_f32 v[32:33], v[32:33], v[144:145] op_sel_hi:[1,0]
	v_pk_mul_f32 v[30:31], v[30:31], v[144:145] op_sel_hi:[1,0]
	v_pk_mul_f32 v[28:29], v[28:29], v[144:145] op_sel_hi:[1,0]
	v_pk_mul_f32 v[26:27], v[26:27], v[144:145] op_sel_hi:[1,0]
	v_pk_mul_f32 v[24:25], v[24:25], v[144:145] op_sel_hi:[1,0]
	v_pk_mul_f32 v[22:23], v[22:23], v[144:145] op_sel_hi:[1,0]
	v_pk_mul_f32 v[20:21], v[20:21], v[144:145] op_sel_hi:[1,0]
.LBB6_1278:
	v_cndmask_b32_e32 v135, v154, v135, vcc
	v_mov_b32_e32 v238, v135
	v_pk_fma_f32 v[98:99], v[98:99], s[42:43], v[238:239] op_sel_hi:[1,0,0] neg_lo:[0,0,1] neg_hi:[0,0,1]
	v_pk_fma_f32 v[96:97], v[96:97], s[42:43], v[238:239] op_sel_hi:[1,0,0] neg_lo:[0,0,1] neg_hi:[0,0,1]
	v_pk_fma_f32 v[94:95], v[94:95], s[42:43], v[238:239] op_sel_hi:[1,0,0] neg_lo:[0,0,1] neg_hi:[0,0,1]
	v_pk_fma_f32 v[92:93], v[92:93], s[42:43], v[238:239] op_sel_hi:[1,0,0] neg_lo:[0,0,1] neg_hi:[0,0,1]
	v_pk_fma_f32 v[90:91], v[90:91], s[42:43], v[238:239] op_sel_hi:[1,0,0] neg_lo:[0,0,1] neg_hi:[0,0,1]
	v_pk_fma_f32 v[88:89], v[88:89], s[42:43], v[238:239] op_sel_hi:[1,0,0] neg_lo:[0,0,1] neg_hi:[0,0,1]
	v_pk_fma_f32 v[86:87], v[86:87], s[42:43], v[238:239] op_sel_hi:[1,0,0] neg_lo:[0,0,1] neg_hi:[0,0,1]
	v_pk_fma_f32 v[84:85], v[84:85], s[42:43], v[238:239] op_sel_hi:[1,0,0] neg_lo:[0,0,1] neg_hi:[0,0,1]
	v_pk_fma_f32 v[216:217], v[82:83], s[42:43], v[238:239] op_sel_hi:[1,0,0] neg_lo:[0,0,1] neg_hi:[0,0,1]
	v_pk_fma_f32 v[218:219], v[80:81], s[42:43], v[238:239] op_sel_hi:[1,0,0] neg_lo:[0,0,1] neg_hi:[0,0,1]
	v_pk_fma_f32 v[220:221], v[78:79], s[42:43], v[238:239] op_sel_hi:[1,0,0] neg_lo:[0,0,1] neg_hi:[0,0,1]
	v_pk_fma_f32 v[222:223], v[76:77], s[42:43], v[238:239] op_sel_hi:[1,0,0] neg_lo:[0,0,1] neg_hi:[0,0,1]
	v_pk_fma_f32 v[230:231], v[68:69], s[42:43], v[238:239] op_sel_hi:[1,0,0] neg_lo:[0,0,1] neg_hi:[0,0,1]
	v_pk_fma_f32 v[232:233], v[70:71], s[42:43], v[238:239] op_sel_hi:[1,0,0] neg_lo:[0,0,1] neg_hi:[0,0,1]
	v_pk_fma_f32 v[234:235], v[72:73], s[42:43], v[238:239] op_sel_hi:[1,0,0] neg_lo:[0,0,1] neg_hi:[0,0,1]
	v_pk_fma_f32 v[236:237], v[74:75], s[42:43], v[238:239] op_sel_hi:[1,0,0] neg_lo:[0,0,1] neg_hi:[0,0,1]
	v_exp_f32_e32 v68, v84
	v_exp_f32_e32 v76, v230
	v_exp_f32_e32 v69, v85
	v_exp_f32_e32 v77, v231
	v_exp_f32_e32 v70, v86
	v_exp_f32_e32 v78, v232
	v_exp_f32_e32 v71, v87
	v_exp_f32_e32 v79, v233
	v_exp_f32_e32 v72, v88
	v_exp_f32_e32 v80, v234
	v_exp_f32_e32 v73, v89
	v_exp_f32_e32 v81, v235
	v_exp_f32_e32 v74, v90
	v_exp_f32_e32 v82, v236
	v_exp_f32_e32 v75, v91
	v_exp_f32_e32 v83, v237
	v_exp_f32_e32 v84, v92
	v_exp_f32_e32 v86, v222
	v_exp_f32_e32 v85, v93
	v_exp_f32_e32 v87, v223
	v_exp_f32_e32 v88, v94
	v_exp_f32_e32 v90, v220
	v_exp_f32_e32 v89, v95
	v_exp_f32_e32 v91, v221
	v_exp_f32_e32 v92, v96
	v_exp_f32_e32 v94, v218
	v_exp_f32_e32 v93, v97
	v_exp_f32_e32 v95, v219
	v_exp_f32_e32 v96, v98
	v_exp_f32_e32 v98, v216
	v_exp_f32_e32 v97, v99
	v_exp_f32_e32 v99, v217
	v_pk_add_f32 v[154:155], v[90:91], v[88:89]
	v_pk_add_f32 v[156:157], v[78:79], v[70:71]
	v_pk_add_f32 v[160:161], v[82:83], v[74:75]
	v_pk_add_f32 v[158:159], v[98:99], v[96:97]
	v_pk_add_f32 v[162:163], v[86:87], v[84:85]
	v_pk_add_f32 v[164:165], v[76:77], v[68:69]
	v_pk_add_f32 v[166:167], v[94:95], v[92:93]
	v_pk_add_f32 v[168:169], v[80:81], v[72:73]
	v_pk_add_f32 v[162:163], v[164:165], v[162:163]
	v_pk_add_f32 v[166:167], v[168:169], v[166:167]
	v_pk_add_f32 v[158:159], v[160:161], v[158:159]
	v_pk_add_f32 v[154:155], v[156:157], v[154:155]
	v_pk_add_f32 v[156:157], v[162:163], v[166:167]
	v_pk_add_f32 v[154:155], v[154:155], v[158:159]
	v_cndmask_b32_e64 v144, v144, 1.0, vcc
	v_pk_add_f32 v[154:155], v[156:157], v[154:155]
	v_cvt_pk_bf16_f32 v68, v68, v69
	v_add_f32_e32 v170, v154, v155
	v_fmac_f32_e32 v170, v183, v144
	v_cvt_pk_bf16_f32 v69, v70, v71
	v_cvt_pk_bf16_f32 v71, v74, v75
	v_cvt_pk_bf16_f32 v75, v96, v97
	v_add3_u32 v96, s13, v133, v2
	v_add3_u32 v144, s13, v2, v133
	v_cvt_pk_bf16_f32 v70, v72, v73
	v_cvt_pk_bf16_f32 v72, v84, v85
	v_cvt_pk_bf16_f32 v73, v88, v89
	v_cvt_pk_bf16_f32 v74, v92, v93
	v_cvt_pk_bf16_f32 v76, v76, v77
	v_cvt_pk_bf16_f32 v77, v78, v79
	v_cvt_pk_bf16_f32 v78, v80, v81
	v_cvt_pk_bf16_f32 v79, v82, v83
	v_cvt_pk_bf16_f32 v80, v86, v87
	v_cvt_pk_bf16_f32 v81, v90, v91
	v_cvt_pk_bf16_f32 v82, v94, v95
	v_cvt_pk_bf16_f32 v83, v98, v99
	ds_read_b128 v[84:87], v96 offset:9216
	ds_read_b128 v[88:91], v96 offset:9248
	ds_read_b128 v[92:95], v96 offset:9280
	ds_read_b128 v[96:99], v96 offset:9312
	ds_read_b128 v[154:157], v144 offset:13824
	ds_read_b128 v[158:161], v144 offset:13856
	ds_read_b128 v[162:165], v144 offset:13888
	ds_read_b128 v[166:169], v144 offset:13920
	s_waitcnt lgkmcnt(7)
	v_mfma_f32_32x32x16_bf16 v[4:19], v[84:87], v[68:71], v[4:19]
	s_waitcnt lgkmcnt(6)
	v_mfma_f32_32x32x16_bf16 v[4:19], v[88:91], v[72:75], v[4:19]
	s_waitcnt lgkmcnt(5)
	v_mfma_f32_32x32x16_bf16 v[4:19], v[92:95], v[76:79], v[4:19]
	s_waitcnt lgkmcnt(4)
	v_mfma_f32_32x32x16_bf16 v[4:19], v[96:99], v[80:83], v[4:19]
	ds_read_b128 v[84:87], v144 offset:18432
	ds_read_b128 v[88:91], v144 offset:18464
	ds_read_b128 v[92:95], v144 offset:18496
	ds_read_b128 v[96:99], v144 offset:18528
	s_waitcnt lgkmcnt(7)
	v_mfma_f32_32x32x16_bf16 v[52:67], v[154:157], v[68:71], v[52:67]
	s_waitcnt lgkmcnt(6)
	v_mfma_f32_32x32x16_bf16 v[52:67], v[158:161], v[72:75], v[52:67]
	s_waitcnt lgkmcnt(5)
	v_mfma_f32_32x32x16_bf16 v[52:67], v[162:165], v[76:79], v[52:67]
	s_waitcnt lgkmcnt(4)
	v_mfma_f32_32x32x16_bf16 v[52:67], v[166:169], v[80:83], v[52:67]
	ds_read_b128 v[154:157], v144 offset:23040
	ds_read_b128 v[158:161], v144 offset:23072
	ds_read_b128 v[162:165], v144 offset:23104
	ds_read_b128 v[166:169], v144 offset:23136
	s_waitcnt lgkmcnt(7)
	v_mfma_f32_32x32x16_bf16 v[36:51], v[84:87], v[68:71], v[36:51]
	s_waitcnt lgkmcnt(6)
	v_mfma_f32_32x32x16_bf16 v[36:51], v[88:91], v[72:75], v[36:51]
	s_waitcnt lgkmcnt(5)
	v_mfma_f32_32x32x16_bf16 v[36:51], v[92:95], v[76:79], v[36:51]
	s_waitcnt lgkmcnt(4)
	v_mfma_f32_32x32x16_bf16 v[36:51], v[96:99], v[80:83], v[36:51]
	s_waitcnt lgkmcnt(3)
	v_mfma_f32_32x32x16_bf16 v[20:35], v[154:157], v[68:71], v[20:35]
	s_waitcnt lgkmcnt(2)
	v_mfma_f32_32x32x16_bf16 v[20:35], v[158:161], v[72:75], v[20:35]
	s_waitcnt lgkmcnt(1)
	v_mfma_f32_32x32x16_bf16 v[20:35], v[162:165], v[76:79], v[20:35]
	s_waitcnt lgkmcnt(0)
	v_mfma_f32_32x32x16_bf16 v[20:35], v[166:169], v[80:83], v[20:35]
	v_mov_b32_e32 v183, v170

.LBB6_1284:
	s_nop 8
	s_nop 4
	s_nop 0
	v_max_f32_e32 v103, v91, v75
	v_max_f32_e32 v100, v88, v72
	v_max_f32_e32 v101, v89, v73
	v_max_f32_e32 v102, v90, v74
	v_max3_f32 v103, v87, v71, v103
	v_max3_f32 v100, v84, v68, v100
	v_max3_f32 v101, v85, v69, v101
	v_max3_f32 v102, v86, v70, v102
	v_max3_f32 v103, v95, v79, v103
	v_max3_f32 v100, v92, v76, v100
	v_max3_f32 v101, v93, v77, v101
	v_max3_f32 v102, v94, v78, v102
	v_max_f32_e32 v104, v98, v82
	v_max3_f32 v103, v99, v83, v103
	v_max3_f32 v100, v96, v80, v100
	v_max3_f32 v101, v97, v81, v101
	v_max3_f32 v102, v104, v102, v103
	v_max3_f32 v100, v100, v101, v102
	v_mov_b32_e32 v101, v100
	s_nop 1
	v_permlane32_swap_b32_e32 v100, v101
	v_max_f32_e32 v101, v101, v101
	v_max_f32_e32 v100, v100, v100
	v_max_f32_e32 v100, v100, v101
	v_mul_f32_e32 v100, s42, v100
	v_sub_f32_e32 v101, v100, v135
	v_cmp_ge_f32_e32 vcc, s97, v101
	v_max_f32_e32 v101, v135, v135
	v_max_f32_e32 v101, v101, v100
	v_sub_f32_e32 v100, v135, v101
	v_exp_f32_e32 v100, v100
	s_cmp_eq_u64 vcc, exec
	s_cselect_b64 vcc, -1, 0
	s_cbranch_vccnz .LBB6_1286
	v_pk_mul_f32 v[18:19], v[18:19], v[100:101] op_sel_hi:[1,0]
	v_pk_mul_f32 v[16:17], v[16:17], v[100:101] op_sel_hi:[1,0]
	v_pk_mul_f32 v[14:15], v[14:15], v[100:101] op_sel_hi:[1,0]
	v_pk_mul_f32 v[12:13], v[12:13], v[100:101] op_sel_hi:[1,0]
	v_pk_mul_f32 v[10:11], v[10:11], v[100:101] op_sel_hi:[1,0]
	v_pk_mul_f32 v[8:9], v[8:9], v[100:101] op_sel_hi:[1,0]
	v_pk_mul_f32 v[6:7], v[6:7], v[100:101] op_sel_hi:[1,0]
	v_pk_mul_f32 v[4:5], v[4:5], v[100:101] op_sel_hi:[1,0]
	v_pk_mul_f32 v[66:67], v[66:67], v[100:101] op_sel_hi:[1,0]
	v_pk_mul_f32 v[64:65], v[64:65], v[100:101] op_sel_hi:[1,0]
	v_pk_mul_f32 v[62:63], v[62:63], v[100:101] op_sel_hi:[1,0]
	v_pk_mul_f32 v[60:61], v[60:61], v[100:101] op_sel_hi:[1,0]
	v_pk_mul_f32 v[58:59], v[58:59], v[100:101] op_sel_hi:[1,0]
	v_pk_mul_f32 v[56:57], v[56:57], v[100:101] op_sel_hi:[1,0]
	v_pk_mul_f32 v[54:55], v[54:55], v[100:101] op_sel_hi:[1,0]
	v_pk_mul_f32 v[52:53], v[52:53], v[100:101] op_sel_hi:[1,0]
	v_pk_mul_f32 v[50:51], v[50:51], v[100:101] op_sel_hi:[1,0]
	v_pk_mul_f32 v[48:49], v[48:49], v[100:101] op_sel_hi:[1,0]
	v_pk_mul_f32 v[46:47], v[46:47], v[100:101] op_sel_hi:[1,0]
	v_pk_mul_f32 v[44:45], v[44:45], v[100:101] op_sel_hi:[1,0]
	v_pk_mul_f32 v[42:43], v[42:43], v[100:101] op_sel_hi:[1,0]
	v_pk_mul_f32 v[40:41], v[40:41], v[100:101] op_sel_hi:[1,0]
	v_pk_mul_f32 v[38:39], v[38:39], v[100:101] op_sel_hi:[1,0]
	v_pk_mul_f32 v[36:37], v[36:37], v[100:101] op_sel_hi:[1,0]
	v_pk_mul_f32 v[34:35], v[34:35], v[100:101] op_sel_hi:[1,0]
	v_pk_mul_f32 v[32:33], v[32:33], v[100:101] op_sel_hi:[1,0]
	v_pk_mul_f32 v[30:31], v[30:31], v[100:101] op_sel_hi:[1,0]
	v_pk_mul_f32 v[28:29], v[28:29], v[100:101] op_sel_hi:[1,0]
	v_pk_mul_f32 v[26:27], v[26:27], v[100:101] op_sel_hi:[1,0]
	v_pk_mul_f32 v[24:25], v[24:25], v[100:101] op_sel_hi:[1,0]
	v_pk_mul_f32 v[22:23], v[22:23], v[100:101] op_sel_hi:[1,0]
	v_pk_mul_f32 v[20:21], v[20:21], v[100:101] op_sel_hi:[1,0]
.LBB6_1286:
	v_cndmask_b32_e32 v101, v101, v135, vcc
	v_cndmask_b32_e64 v116, v100, 1.0, vcc
	v_mov_b32_e32 v238, v101
	v_pk_fma_f32 v[98:99], v[98:99], s[42:43], v[238:239] op_sel_hi:[1,0,0] neg_lo:[0,0,1] neg_hi:[0,0,1]
	v_pk_fma_f32 v[96:97], v[96:97], s[42:43], v[238:239] op_sel_hi:[1,0,0] neg_lo:[0,0,1] neg_hi:[0,0,1]
	v_pk_fma_f32 v[94:95], v[94:95], s[42:43], v[238:239] op_sel_hi:[1,0,0] neg_lo:[0,0,1] neg_hi:[0,0,1]
	v_pk_fma_f32 v[92:93], v[92:93], s[42:43], v[238:239] op_sel_hi:[1,0,0] neg_lo:[0,0,1] neg_hi:[0,0,1]
	v_pk_fma_f32 v[90:91], v[90:91], s[42:43], v[238:239] op_sel_hi:[1,0,0] neg_lo:[0,0,1] neg_hi:[0,0,1]
	v_pk_fma_f32 v[88:89], v[88:89], s[42:43], v[238:239] op_sel_hi:[1,0,0] neg_lo:[0,0,1] neg_hi:[0,0,1]
	v_pk_fma_f32 v[86:87], v[86:87], s[42:43], v[238:239] op_sel_hi:[1,0,0] neg_lo:[0,0,1] neg_hi:[0,0,1]
	v_pk_fma_f32 v[84:85], v[84:85], s[42:43], v[238:239] op_sel_hi:[1,0,0] neg_lo:[0,0,1] neg_hi:[0,0,1]
	v_pk_fma_f32 v[216:217], v[82:83], s[42:43], v[238:239] op_sel_hi:[1,0,0] neg_lo:[0,0,1] neg_hi:[0,0,1]
	v_pk_fma_f32 v[218:219], v[80:81], s[42:43], v[238:239] op_sel_hi:[1,0,0] neg_lo:[0,0,1] neg_hi:[0,0,1]
	v_pk_fma_f32 v[220:221], v[78:79], s[42:43], v[238:239] op_sel_hi:[1,0,0] neg_lo:[0,0,1] neg_hi:[0,0,1]
	v_pk_fma_f32 v[222:223], v[76:77], s[42:43], v[238:239] op_sel_hi:[1,0,0] neg_lo:[0,0,1] neg_hi:[0,0,1]
	v_pk_fma_f32 v[230:231], v[68:69], s[42:43], v[238:239] op_sel_hi:[1,0,0] neg_lo:[0,0,1] neg_hi:[0,0,1]
	v_pk_fma_f32 v[232:233], v[70:71], s[42:43], v[238:239] op_sel_hi:[1,0,0] neg_lo:[0,0,1] neg_hi:[0,0,1]
	v_pk_fma_f32 v[234:235], v[72:73], s[42:43], v[238:239] op_sel_hi:[1,0,0] neg_lo:[0,0,1] neg_hi:[0,0,1]
	v_pk_fma_f32 v[236:237], v[74:75], s[42:43], v[238:239] op_sel_hi:[1,0,0] neg_lo:[0,0,1] neg_hi:[0,0,1]
	v_exp_f32_e32 v68, v84
	v_exp_f32_e32 v76, v230
	v_exp_f32_e32 v69, v85
	v_exp_f32_e32 v77, v231
	v_exp_f32_e32 v70, v86
	v_exp_f32_e32 v78, v232
	v_exp_f32_e32 v71, v87
	v_exp_f32_e32 v79, v233
	v_exp_f32_e32 v72, v88
	v_exp_f32_e32 v80, v234
	v_exp_f32_e32 v73, v89
	v_exp_f32_e32 v81, v235
	v_exp_f32_e32 v74, v90
	v_exp_f32_e32 v82, v236
	v_exp_f32_e32 v75, v91
	v_exp_f32_e32 v83, v237
	v_exp_f32_e32 v84, v92
	v_exp_f32_e32 v86, v222
	v_exp_f32_e32 v85, v93
	v_exp_f32_e32 v87, v223
	v_exp_f32_e32 v88, v94
	v_exp_f32_e32 v90, v220
	v_exp_f32_e32 v89, v95
	v_exp_f32_e32 v91, v221
	v_exp_f32_e32 v92, v96
	v_exp_f32_e32 v94, v218
	v_exp_f32_e32 v93, v97
	v_exp_f32_e32 v95, v219
	v_exp_f32_e32 v96, v98
	v_exp_f32_e32 v98, v216
	v_exp_f32_e32 v97, v99
	v_exp_f32_e32 v99, v217
	v_pk_add_f32 v[100:101], v[90:91], v[88:89]
	v_pk_add_f32 v[102:103], v[78:79], v[70:71]
	v_pk_add_f32 v[106:107], v[82:83], v[74:75]
	v_pk_add_f32 v[104:105], v[98:99], v[96:97]
	v_pk_add_f32 v[108:109], v[86:87], v[84:85]
	v_pk_add_f32 v[110:111], v[76:77], v[68:69]
	v_pk_add_f32 v[112:113], v[94:95], v[92:93]
	v_pk_add_f32 v[114:115], v[80:81], v[72:73]
	v_pk_add_f32 v[108:109], v[110:111], v[108:109]
	v_pk_add_f32 v[112:113], v[114:115], v[112:113]
	v_pk_add_f32 v[104:105], v[106:107], v[104:105]
	v_pk_add_f32 v[100:101], v[102:103], v[100:101]
	v_pk_add_f32 v[102:103], v[108:109], v[112:113]
	v_pk_add_f32 v[100:101], v[100:101], v[104:105]
	v_cvt_pk_bf16_f32 v68, v68, v69
	v_pk_add_f32 v[100:101], v[102:103], v[100:101]
	v_cvt_pk_bf16_f32 v69, v70, v71
	v_cvt_pk_bf16_f32 v71, v74, v75
	v_cvt_pk_bf16_f32 v75, v96, v97
	v_add3_u32 v96, s1, v133, v2
	v_add3_u32 v2, s1, v2, v133
	v_add_f32_e32 v117, v100, v101
	v_cvt_pk_bf16_f32 v70, v72, v73
	v_cvt_pk_bf16_f32 v72, v84, v85
	v_cvt_pk_bf16_f32 v73, v88, v89
	v_cvt_pk_bf16_f32 v74, v92, v93
	v_cvt_pk_bf16_f32 v76, v76, v77
	v_cvt_pk_bf16_f32 v77, v78, v79
	v_cvt_pk_bf16_f32 v78, v80, v81
	v_cvt_pk_bf16_f32 v79, v82, v83
	v_cvt_pk_bf16_f32 v80, v86, v87
	v_cvt_pk_bf16_f32 v81, v90, v91
	v_cvt_pk_bf16_f32 v82, v94, v95
	v_cvt_pk_bf16_f32 v83, v98, v99
	ds_read_b128 v[84:87], v96 offset:9216
	ds_read_b128 v[88:91], v96 offset:9248
	ds_read_b128 v[92:95], v96 offset:9280
	ds_read_b128 v[96:99], v96 offset:9312
	ds_read_b128 v[100:103], v2 offset:13824
	ds_read_b128 v[104:107], v2 offset:13856
	ds_read_b128 v[108:111], v2 offset:13888
	ds_read_b128 v[112:115], v2 offset:13920
	v_fmac_f32_e32 v117, v183, v116
	s_waitcnt lgkmcnt(7)
	v_mfma_f32_32x32x16_bf16 v[4:19], v[84:87], v[68:71], v[4:19]
	s_waitcnt lgkmcnt(6)
	v_mfma_f32_32x32x16_bf16 v[4:19], v[88:91], v[72:75], v[4:19]
	s_waitcnt lgkmcnt(5)
	v_mfma_f32_32x32x16_bf16 v[4:19], v[92:95], v[76:79], v[4:19]
	s_waitcnt lgkmcnt(4)
	v_mfma_f32_32x32x16_bf16 v[4:19], v[96:99], v[80:83], v[4:19]
	ds_read_b128 v[84:87], v2 offset:18432
	ds_read_b128 v[88:91], v2 offset:18464
	ds_read_b128 v[92:95], v2 offset:18496
	ds_read_b128 v[96:99], v2 offset:18528
	s_waitcnt lgkmcnt(7)
	v_mfma_f32_32x32x16_bf16 v[52:67], v[100:103], v[68:71], v[52:67]
	s_waitcnt lgkmcnt(6)
	v_mfma_f32_32x32x16_bf16 v[52:67], v[104:107], v[72:75], v[52:67]
	s_waitcnt lgkmcnt(5)
	v_mfma_f32_32x32x16_bf16 v[52:67], v[108:111], v[76:79], v[52:67]
	s_waitcnt lgkmcnt(4)
	v_mfma_f32_32x32x16_bf16 v[52:67], v[112:115], v[80:83], v[52:67]
	ds_read_b128 v[100:103], v2 offset:23040
	ds_read_b128 v[104:107], v2 offset:23072
	ds_read_b128 v[108:111], v2 offset:23104
	ds_read_b128 v[112:115], v2 offset:23136
	s_waitcnt lgkmcnt(7)
	v_mfma_f32_32x32x16_bf16 v[36:51], v[84:87], v[68:71], v[36:51]
	s_waitcnt lgkmcnt(6)
	v_mfma_f32_32x32x16_bf16 v[36:51], v[88:91], v[72:75], v[36:51]
	s_waitcnt lgkmcnt(5)
	v_mfma_f32_32x32x16_bf16 v[36:51], v[92:95], v[76:79], v[36:51]
	s_waitcnt lgkmcnt(4)
	v_mfma_f32_32x32x16_bf16 v[36:51], v[96:99], v[80:83], v[36:51]
	s_waitcnt lgkmcnt(3)
	v_mfma_f32_32x32x16_bf16 v[20:35], v[100:103], v[68:71], v[20:35]
	s_waitcnt lgkmcnt(2)
	v_mfma_f32_32x32x16_bf16 v[20:35], v[104:107], v[72:75], v[20:35]
	s_waitcnt lgkmcnt(1)
	v_mfma_f32_32x32x16_bf16 v[20:35], v[108:111], v[76:79], v[20:35]
	s_waitcnt lgkmcnt(0)
	v_mfma_f32_32x32x16_bf16 v[20:35], v[112:115], v[80:83], v[20:35]
	v_mov_b32_e32 v183, v117
